# speedup vs baseline: 1.0139x; 1.0139x over previous
_Z12final_kernelPKDF16_S0_PKfS2_S2_S2_Pf:
	s_load_dwordx8 s[4:11], s[0:1], 0x0
	s_load_dwordx2 s[14:15], s[0:1], 0x20
	s_load_dwordx4 s[16:19], s[0:1], 0x28
	v_readfirstlane_b32 s3, v0
	v_bfe_u32 v70, v0, 4, 2
	v_and_b32_e32 v71, 15, v0
	s_lshr_b32 s3, s3, 6
	s_lshl_b32 s12, s2, 4
	s_lshl_b32 s20, s2, 11
	s_lshl_b32 s21, s3, 7
	s_lshl_b32 s22, s3, 6
	v_lshlrev_b32_e32 v72, 7, v71
	v_lshl_or_b32 v72, v70, 5, v72
	v_lshlrev_b32_e32 v73, 12, v70
	v_lshl_or_b32 v73, v71, 3, v73
	v_lshlrev_b32_e32 v74, 3, v71
	v_lshlrev_b32_e32 v75, 9, v70
	v_lshl_or_b32 v75, v71, 2, v75
	s_add_i32 s23, s22, 0x1080
	v_lshl_add_u32 v76, v70, 4, s23
	s_waitcnt lgkmcnt(0)
	s_load_dword s13, s[16:17], 0x0
	s_add_u32 s4, s4, s20
	s_addc_u32 s5, s5, 0
	s_add_u32 s8, s8, s21
	s_addc_u32 s9, s9, 0
	global_load_dwordx4 v[2:5], v72, s[4:5] nt
	global_load_dwordx4 v[6:9], v72, s[4:5] offset:16 nt
	global_load_dwordx2 v[26:27], v73, s[8:9]
	global_load_dwordx2 v[28:29], v73, s[8:9] offset:256
	global_load_dwordx2 v[30:31], v73, s[8:9] offset:512
	global_load_dwordx2 v[32:33], v73, s[8:9] offset:768
	global_load_dwordx2 v[34:35], v73, s[8:9] offset:1024
	global_load_dwordx2 v[36:37], v73, s[8:9] offset:1280
	global_load_dwordx2 v[38:39], v73, s[8:9] offset:1536
	global_load_dwordx2 v[40:41], v73, s[8:9] offset:1792
	global_load_dwordx2 v[42:43], v73, s[8:9] offset:2048
	global_load_dwordx2 v[44:45], v73, s[8:9] offset:2304
	global_load_dwordx2 v[46:47], v73, s[8:9] offset:2560
	global_load_dwordx2 v[48:49], v73, s[8:9] offset:2816
	global_load_dwordx2 v[50:51], v73, s[8:9] offset:3072
	global_load_dwordx2 v[52:53], v73, s[8:9] offset:3328
	global_load_dwordx2 v[54:55], v73, s[8:9] offset:3584
	global_load_dwordx2 v[56:57], v73, s[8:9] offset:3840
	s_add_u32 s6, s6, s20
	s_addc_u32 s7, s7, 0
	s_add_u32 s6, s6, s22
	s_addc_u32 s7, s7, 0
	global_load_dword v60, v75, s[6:7] nt
	global_load_dword v61, v75, s[6:7] offset:128 nt
	global_load_dword v62, v75, s[6:7] offset:256 nt
	global_load_dword v63, v75, s[6:7] offset:384 nt
	s_add_u32 s10, s10, s21
	s_addc_u32 s11, s11, 0
	global_load_dwordx2 v[58:59], v74, s[10:11]
	s_add_u32 s14, s14, s21
	s_addc_u32 s15, s15, 0
	global_load_dwordx2 v[68:69], v74, s[14:15]
	s_waitcnt vmcnt(22)
	v_cvt_f32_f16_e32 v10, v2
	v_max_f32_e32 v10, 0, v10
	v_cvt_f32_f16_sdwa v11, v2 dst_sel:DWORD dst_unused:UNUSED_PAD src0_sel:WORD_1
	v_max_f32_e32 v11, 0, v11
	s_waitcnt vmcnt(21)
	v_mfma_f32_16x16x4_f32 a[0:3], v10, v26, 0
	v_cvt_f32_f16_e32 v12, v3
	v_max_f32_e32 v12, 0, v12
	v_mfma_f32_16x16x4_f32 a[4:7], v10, v27, 0
	s_waitcnt vmcnt(20)
	v_mfma_f32_16x16x4_f32 a[0:3], v11, v28, a[0:3]
	v_cvt_f32_f16_sdwa v13, v3 dst_sel:DWORD dst_unused:UNUSED_PAD src0_sel:WORD_1
	v_max_f32_e32 v13, 0, v13
	v_mfma_f32_16x16x4_f32 a[4:7], v11, v29, a[4:7]
	s_waitcnt vmcnt(19)
	v_mfma_f32_16x16x4_f32 a[0:3], v12, v30, a[0:3]
	v_cvt_f32_f16_e32 v14, v4
	v_max_f32_e32 v14, 0, v14
	v_mfma_f32_16x16x4_f32 a[4:7], v12, v31, a[4:7]
	s_waitcnt vmcnt(18)
	v_mfma_f32_16x16x4_f32 a[0:3], v13, v32, a[0:3]
	v_cvt_f32_f16_sdwa v15, v4 dst_sel:DWORD dst_unused:UNUSED_PAD src0_sel:WORD_1
	v_max_f32_e32 v15, 0, v15
	v_mfma_f32_16x16x4_f32 a[4:7], v13, v33, a[4:7]
	s_waitcnt vmcnt(17)
	v_mfma_f32_16x16x4_f32 a[0:3], v14, v34, a[0:3]
	v_cvt_f32_f16_e32 v16, v5
	v_max_f32_e32 v16, 0, v16
	v_mfma_f32_16x16x4_f32 a[4:7], v14, v35, a[4:7]
	s_waitcnt vmcnt(16)
	v_mfma_f32_16x16x4_f32 a[0:3], v15, v36, a[0:3]
	v_cvt_f32_f16_sdwa v17, v5 dst_sel:DWORD dst_unused:UNUSED_PAD src0_sel:WORD_1
	v_max_f32_e32 v17, 0, v17
	v_mfma_f32_16x16x4_f32 a[4:7], v15, v37, a[4:7]
	s_waitcnt vmcnt(15)
	v_mfma_f32_16x16x4_f32 a[0:3], v16, v38, a[0:3]
	v_cvt_f32_f16_e32 v18, v6
	v_max_f32_e32 v18, 0, v18
	v_mfma_f32_16x16x4_f32 a[4:7], v16, v39, a[4:7]
	s_waitcnt vmcnt(14)
	v_mfma_f32_16x16x4_f32 a[0:3], v17, v40, a[0:3]
	v_cvt_f32_f16_sdwa v19, v6 dst_sel:DWORD dst_unused:UNUSED_PAD src0_sel:WORD_1
	v_max_f32_e32 v19, 0, v19
	v_mfma_f32_16x16x4_f32 a[4:7], v17, v41, a[4:7]
	s_waitcnt vmcnt(13)
	v_mfma_f32_16x16x4_f32 a[0:3], v18, v42, a[0:3]
	v_cvt_f32_f16_e32 v20, v7
	v_max_f32_e32 v20, 0, v20
	v_mfma_f32_16x16x4_f32 a[4:7], v18, v43, a[4:7]
	s_waitcnt vmcnt(12)
	v_mfma_f32_16x16x4_f32 a[0:3], v19, v44, a[0:3]
	v_cvt_f32_f16_sdwa v21, v7 dst_sel:DWORD dst_unused:UNUSED_PAD src0_sel:WORD_1
	v_max_f32_e32 v21, 0, v21
	v_mfma_f32_16x16x4_f32 a[4:7], v19, v45, a[4:7]
	s_waitcnt vmcnt(11)
	v_mfma_f32_16x16x4_f32 a[0:3], v20, v46, a[0:3]
	v_cvt_f32_f16_e32 v22, v8
	v_max_f32_e32 v22, 0, v22
	v_mfma_f32_16x16x4_f32 a[4:7], v20, v47, a[4:7]
	s_waitcnt vmcnt(10)
	v_mfma_f32_16x16x4_f32 a[0:3], v21, v48, a[0:3]
	v_cvt_f32_f16_sdwa v23, v8 dst_sel:DWORD dst_unused:UNUSED_PAD src0_sel:WORD_1
	v_max_f32_e32 v23, 0, v23
	v_mfma_f32_16x16x4_f32 a[4:7], v21, v49, a[4:7]
	s_waitcnt vmcnt(9)
	v_mfma_f32_16x16x4_f32 a[0:3], v22, v50, a[0:3]
	v_cvt_f32_f16_e32 v24, v9
	v_max_f32_e32 v24, 0, v24
	v_mfma_f32_16x16x4_f32 a[4:7], v22, v51, a[4:7]
	s_waitcnt vmcnt(8)
	v_mfma_f32_16x16x4_f32 a[0:3], v23, v52, a[0:3]
	v_cvt_f32_f16_sdwa v25, v9 dst_sel:DWORD dst_unused:UNUSED_PAD src0_sel:WORD_1
	v_max_f32_e32 v25, 0, v25
	v_mfma_f32_16x16x4_f32 a[4:7], v23, v53, a[4:7]
	s_waitcnt vmcnt(7)
	v_mfma_f32_16x16x4_f32 a[0:3], v24, v54, a[0:3]
	v_mfma_f32_16x16x4_f32 a[4:7], v24, v55, a[4:7]
	s_waitcnt vmcnt(6)
	v_mfma_f32_16x16x4_f32 a[0:3], v25, v56, a[0:3]
	v_mfma_f32_16x16x4_f32 a[4:7], v25, v57, a[4:7]
	v_cmp_eq_u32_e32 vcc, 0, v71
	s_waitcnt vmcnt(0)
	v_cvt_f32_f16_sdwa v64, v60 dst_sel:DWORD dst_unused:UNUSED_PAD src0_sel:WORD_1
	v_cvt_f32_f16_sdwa v65, v61 dst_sel:DWORD dst_unused:UNUSED_PAD src0_sel:WORD_1
	v_cvt_f32_f16_sdwa v66, v62 dst_sel:DWORD dst_unused:UNUSED_PAD src0_sel:WORD_1
	v_cvt_f32_f16_sdwa v67, v63 dst_sel:DWORD dst_unused:UNUSED_PAD src0_sel:WORD_1
	v_cvt_f32_f16_e32 v60, v60
	v_cvt_f32_f16_e32 v61, v61
	v_cvt_f32_f16_e32 v62, v62
	v_cvt_f32_f16_e32 v63, v63
	v_add_f32_e32 v60, v58, v60
	v_add_f32_e32 v64, v59, v64
	v_add_f32_e32 v61, v58, v61
	v_add_f32_e32 v65, v59, v65
	v_add_f32_e32 v62, v58, v62
	v_add_f32_e32 v66, v59, v66
	v_add_f32_e32 v63, v58, v63
	v_add_f32_e32 v67, v59, v67
	s_nop 1
	v_accvgpr_read_b32 v2, a0
	v_accvgpr_read_b32 v3, a1
	v_accvgpr_read_b32 v4, a2
	v_accvgpr_read_b32 v5, a3
	v_accvgpr_read_b32 v6, a4
	v_accvgpr_read_b32 v7, a5
	v_accvgpr_read_b32 v8, a6
	v_accvgpr_read_b32 v9, a7
	v_add_f32_e32 v2, v2, v60
	v_add_f32_e32 v3, v3, v61
	v_add_f32_e32 v4, v4, v62
	v_add_f32_e32 v5, v5, v63
	v_add_f32_e32 v6, v6, v64
	v_add_f32_e32 v7, v7, v65
	v_add_f32_e32 v8, v8, v66
	v_add_f32_e32 v9, v9, v67
	v_max_f32_e32 v2, 0, v2
	v_max_f32_e32 v3, 0, v3
	v_max_f32_e32 v4, 0, v4
	v_max_f32_e32 v5, 0, v5
	v_max_f32_e32 v6, 0, v6
	v_max_f32_e32 v7, 0, v7
	v_max_f32_e32 v8, 0, v8
	v_max_f32_e32 v9, 0, v9
	v_mul_f32_e32 v6, v69, v6
	v_mul_f32_e32 v7, v69, v7
	v_mul_f32_e32 v8, v69, v8
	v_mul_f32_e32 v9, v69, v9
	v_fmac_f32_e32 v6, v68, v2
	v_fmac_f32_e32 v7, v68, v3
	v_fmac_f32_e32 v8, v68, v4
	v_fmac_f32_e32 v9, v68, v5
	v_add_f32_dpp v6, v6, v6 quad_perm:[1,0,3,2] row_mask:0xf bank_mask:0xf
	v_add_f32_dpp v7, v7, v7 quad_perm:[1,0,3,2] row_mask:0xf bank_mask:0xf
	v_add_f32_dpp v8, v8, v8 quad_perm:[1,0,3,2] row_mask:0xf bank_mask:0xf
	v_add_f32_dpp v9, v9, v9 quad_perm:[1,0,3,2] row_mask:0xf bank_mask:0xf
	v_add_f32_dpp v6, v6, v6 quad_perm:[2,3,0,1] row_mask:0xf bank_mask:0xf
	v_add_f32_dpp v7, v7, v7 quad_perm:[2,3,0,1] row_mask:0xf bank_mask:0xf
	v_add_f32_dpp v8, v8, v8 quad_perm:[2,3,0,1] row_mask:0xf bank_mask:0xf
	v_add_f32_dpp v9, v9, v9 quad_perm:[2,3,0,1] row_mask:0xf bank_mask:0xf
	v_add_f32_dpp v6, v6, v6 row_half_mirror row_mask:0xf bank_mask:0xf
	v_add_f32_dpp v7, v7, v7 row_half_mirror row_mask:0xf bank_mask:0xf
	v_add_f32_dpp v8, v8, v8 row_half_mirror row_mask:0xf bank_mask:0xf
	v_add_f32_dpp v9, v9, v9 row_half_mirror row_mask:0xf bank_mask:0xf
	v_add_f32_dpp v6, v6, v6 row_mirror row_mask:0xf bank_mask:0xf
	v_add_f32_dpp v7, v7, v7 row_mirror row_mask:0xf bank_mask:0xf
	v_add_f32_dpp v8, v8, v8 row_mirror row_mask:0xf bank_mask:0xf
	v_add_f32_dpp v9, v9, v9 row_mirror row_mask:0xf bank_mask:0xf
	s_and_saveexec_b64 s[2:3], vcc
	ds_write_b128 v76, v[6:9]
	s_or_b64 exec, exec, s[2:3]
	v_cmp_gt_u32_e32 vcc, 16, v0
	s_waitcnt lgkmcnt(0)
	s_barrier
	s_and_saveexec_b64 s[2:3], vcc
	s_cbranch_execz .Lfinal_done
	v_lshlrev_b32_e32 v1, 2, v0
	v_add_u32_e32 v1, 0x1000, v1
	ds_read2_b32 v[2:3], v1 offset0:32 offset1:48
	v_or_b32_e32 v0, s12, v0
	v_ashrrev_i32_e32 v1, 31, v0
	v_lshl_add_u64 v[0:1], v[0:1], 2, s[18:19]
	s_waitcnt lgkmcnt(0)
	v_add_f32_e32 v2, v2, v3
	v_add_f32_e32 v2, s13, v2
	global_store_dword v[0:1], v2, off
